# G1: gemm1 (gather) unit header - the four token-row lookups of the next unit issued side by side with one wait instead of four serial LDS+global round trips; on top of B1+E2c+E8b
# speedup vs baseline: 1.0052x; 1.0052x over previous
.LBB0_1404:
	v_cndmask_b32_e64 v129, 0, 1, s[30:31]
	s_xor_b64 s[28:29], s[30:31], -1
	v_cmp_ne_u32_e64 s[0:1], 1, v129
	s_andn2_b64 vcc, exec, s[30:31]
	s_mov_b64 s[30:31], s[26:27]
	s_mov_b64 s[4:5], s[34:35]
	s_cbranch_vccnz .LBB0_1422
	s_add_i32 s23, s53, 0xfffdc000
	s_cmp_gt_i32 s53, 0x23fff
	s_cbranch_scc0 .LG1_gather
	v_add_u32_e32 v129, s23, v146
	v_add_u32_e32 v139, s23, v147
	v_add_u32_e32 v141, s23, v148
	v_add_u32_e32 v142, s23, v149
	s_branch .LBB0_1421
.LG1_gather:
	s_ashr_i32 s36, s53, 8
	s_lshl_b32 s36, s36, 2
	s_add_i32 s36, s36, 0x25200
	v_mov_b32_e32 v208, s36
	ds_read_b32 v208, v208
	s_waitcnt lgkmcnt(0)
	v_lshlrev_b32_e32 v210, 2, v208
	v_add_u32_e32 v211, 0x25000, v210
	ds_read_b32 v211, v211
	v_add_u32_e32 v210, 0x25c80, v210
	ds_read_b32 v210, v210
	v_ashrrev_i32_e32 v209, 31, v208
	v_lshlrev_b64 v[208:209], 16, v[208:209]
	v_lshl_add_u64 v[208:209], s[10:11], 0, v[208:209]
	s_waitcnt lgkmcnt(0)
	v_sub_u32_e32 v211, s53, v211
	v_add_u32_e32 v212, v211, v146
	v_add_u32_e32 v214, v211, v147
	v_add_u32_e32 v216, v211, v148
	v_add_u32_e32 v218, v211, v149
	v_cmp_lt_i32_e64 s[36:37], v212, v210
	v_cmp_lt_i32_e64 s[38:39], v214, v210
	v_cmp_lt_i32_e64 s[58:59], v216, v210
	v_cmp_lt_i32_e64 s[60:61], v218, v210
	s_nop 1
	v_cndmask_b32_e64 v212, 0, v212, s[36:37]
	v_cndmask_b32_e64 v214, 0, v214, s[38:39]
	v_cndmask_b32_e64 v216, 0, v216, s[58:59]
	v_cndmask_b32_e64 v218, 0, v218, s[60:61]
	v_ashrrev_i32_e32 v213, 31, v212
	v_ashrrev_i32_e32 v215, 31, v214
	v_ashrrev_i32_e32 v217, 31, v216
	v_ashrrev_i32_e32 v219, 31, v218
	v_lshl_add_u64 v[212:213], v[212:213], 2, v[208:209]
	v_lshl_add_u64 v[214:215], v[214:215], 2, v[208:209]
	v_lshl_add_u64 v[216:217], v[216:217], 2, v[208:209]
	v_lshl_add_u64 v[218:219], v[218:219], 2, v[208:209]
	global_load_dword v129, v[212:213], off
	global_load_dword v139, v[214:215], off
	global_load_dword v141, v[216:217], off
	global_load_dword v142, v[218:219], off
	s_waitcnt vmcnt(0)
	v_cndmask_b32_e64 v129, 0, v129, s[36:37]
	v_cndmask_b32_e64 v139, 0, v139, s[38:39]
	v_cndmask_b32_e64 v141, 0, v141, s[58:59]
	v_cndmask_b32_e64 v142, 0, v142, s[60:61]
